# v92 + same index-load overlap in the peeled first-tile prologue of the MoE-up phase
# baseline (speedup 1.0000x reference)
;     __device__ __forceinline__ const char* b_ptr(const Gemm& g, const Unit& u) const { return (const char*)g.Bt + (size_t)u.pn * (size_t)BM * g.K * 2; }
;     __device__ __forceinline__ const char* b_ptr(const Gemm& g, const Unit& u) const { return (const char*)g.Bt + ((size_t)u.e * estride + (size_t)u.pn * (size_t)BM * g.K) * 2; }
; #define PG8_STAGE(bufoff, gbase, voff) do { _Pragma("unroll") for (int _i = 0; _i < 2; ++_i) \
;         __builtin_amdgcn_global_load_lds((const unsigned*)((const char*)(gbase) + (voff)[_i]), (LAS unsigned*)(lds + (bufoff) + ldsw + _i * 8192), 16, 0, 0); } while (0)
; #define PG8_WAIT_V(n) asm volatile("s_waitcnt vmcnt(" #n ")" ::: "memory")
; #define PG8_BAR __builtin_amdgcn_s_barrier()
; #define PG8_GLOAD(dst, u) do { if constexpr (GATHER) { _Pragma("unroll") for (int _h = 0; _h < 2; ++_h) _Pragma("unroll") for (int _i = 0; _i < 2; ++_i) dst[_h][_i] = S.row_off(u, _h * HALF + RA[_i], K); } } while (0)
;     __device__ __forceinline__ unsigned row_off(const Unit& u, int vrow, int K) const {
;         const int idx = u.r0 + vrow; int tok = T; if (idx < ecnt[u.e]) tok = elist[(size_t)u.e * T + idx];
;         return (unsigned)tok * (unsigned)(K * 2);
; template <class Epi, class Sched, bool GATHER, bool FP8 = false>
; __device__ __forceinline__ void gemm_phase(LAS unsigned char* lds, const Gemm g, const Sched& S, const Epi& E) {
;     ...
;     const char* cA = GATHER ? (const char*)g.A : (const char*)g.A + (size_t)cur.pm * tstep; const char* cB = S.b_ptr(g, cur);
;     PG8_GLOAD(gc, cur);
;     if constexpr (GATHER) { PG8_WAIT_V(0); }
;     PG8_STAGE(PG8_SB(0, 0), cB, voffB); PG8_STAGE(PG8_SB(0, 1), cB + hstep, voffB); PG8_STAGE_A(PG8_SA(0, 0), cA, 0, false); PG8_STAGE_A(PG8_SA(0, 1), cA, 1, false);
;     if (wr == 1) PG8_BAR;
.LBB0_1400:
	s_add_u32 s19, s94, 0x63200000
	s_addc_u32 s33, s95, 0
	s_lshl_b32 s0, s26, 2
	s_add_i32 s0, s0, 0
	s_add_i32 s0, s0, 0x20b00
	v_mov_b32_e32 v171, 0x7f7f7f7f
	v_mov_b32_e32 v2, s0
	ds_read_b32 v7, v2
	v_bfe_u32 v6, v0, 2, 4
	v_lshrrev_b32_e32 v4, 3, v0
	s_ashr_i32 s27, s26, 31
	v_and_or_b32 v1, v4, 48, v6
	s_lshl_b64 s[0:1], s[26:27], 16
	s_add_u32 s0, s19, s0
	v_add_u32_e32 v2, s6, v1
	s_addc_u32 s1, s33, s1
	s_waitcnt lgkmcnt(0)
	v_cmp_lt_i32_e32 vcc, v2, v7
	v_mov_b32_e32 v180, 0x4000
	v_mov_b32_e32 v164, 0x4000
	s_and_saveexec_b64 s[2:3], vcc
	s_cbranch_execz .LBB0_1402
	v_ashrrev_i32_e32 v3, 31, v2
	v_lshl_add_u64 v[2:3], v[2:3], 2, s[0:1]
	global_load_dword v164, v[2:3], off
.LBB0_1402:
	s_or_b64 exec, exec, s[2:3]
	v_bfe_u32 v2, v0, 3, 25
	v_or_b32_e32 v5, 64, v2
	s_movk_i32 s2, 0x70
	v_and_or_b32 v198, v5, s2, v6
	v_add_u32_e32 v2, s6, v198
	v_cmp_lt_i32_e32 vcc, v2, v7
	s_and_saveexec_b64 s[2:3], vcc
	s_cbranch_execz .LBB0_1404
	v_ashrrev_i32_e32 v3, 31, v2
	v_lshl_add_u64 v[2:3], v[2:3], 2, s[0:1]
	global_load_dword v180, v[2:3], off
.LBB0_1404:
	s_or_b64 exec, exec, s[2:3]
	s_addk_i32 s6, 0x80
	v_add_u32_e32 v2, s6, v1
	v_cmp_lt_i32_e32 vcc, v2, v7
	v_mov_b32_e32 v182, 0x4000
	v_mov_b32_e32 v184, 0x4000
	s_and_saveexec_b64 s[2:3], vcc
	s_cbranch_execz .LBB0_1406
	v_ashrrev_i32_e32 v3, 31, v2
	v_lshl_add_u64 v[2:3], v[2:3], 2, s[0:1]
	global_load_dword v184, v[2:3], off
.LBB0_1406:
	s_or_b64 exec, exec, s[2:3]
	v_add_u32_e32 v2, s6, v198
	v_lshrrev_b32_e32 v9, 2, v0
	v_lshlrev_b32_e32 v6, 4, v0
	v_cmp_lt_i32_e32 vcc, v2, v7
	s_and_saveexec_b64 s[2:3], vcc
	s_cbranch_execz .LBB0_1408
	v_ashrrev_i32_e32 v3, 31, v2
	v_lshl_add_u64 v[2:3], v[2:3], 2, s[0:1]
	global_load_dword v182, v[2:3], off
.LBB0_1408:
	s_or_b64 exec, exec, s[2:3]
	s_waitcnt vmcnt(0)
	v_lshlrev_b32_e32 v164, 11, v164
	v_lshlrev_b32_e32 v180, 11, v180
	v_lshlrev_b32_e32 v184, 11, v184
	v_lshlrev_b32_e32 v182, 11, v182
	s_add_u32 s36, s94, 0x1f00000
	s_addc_u32 s37, s95, 0
	s_ashr_i32 s25, s24, 31
	s_lshl_b64 s[0:1], s[24:25], 19
	v_and_b32_e32 v2, 32, v0
	s_add_u32 s8, s36, s0
	v_bitop3_b32 v7, v6, v2, 48 bitop3:0x6c
	v_lshlrev_b32_e32 v2, 1, v9
	v_lshrrev_b32_e32 v3, 5, v0
	s_addc_u32 s9, s37, s1
	v_and_b32_e32 v2, 24, v2
	v_and_b32_e32 v3, 4, v3
	v_and_b32_e32 v9, 3, v9
	s_add_u32 s6, s94, 0x61100000
	v_or3_b32 v2, v3, v9, v2
	s_movk_i32 s1, 0x60
	s_addc_u32 s7, s95, 0
	v_and_or_b32 v3, v4, 32, v2
	v_and_or_b32 v2, v5, s1, v2
	s_lshr_b32 s1, s14, 6
	s_lshr_b32 s0, s14, 8
	s_lshl_b32 s38, s1, 10
	s_lshl_b64 s[2:3], s[26:27], 23
	v_and_b32_e32 v8, 64, v0
	s_add_u32 s28, s8, s2
	v_or_b32_e32 v166, v7, v8
	s_addc_u32 s29, s9, s3
	s_add_i32 s39, s38, 0
	v_lshl_or_b32 v168, v3, 11, v166
	s_waitcnt vmcnt(0)
	s_add_i32 m0, s39, 0x10000
	v_lshl_or_b32 v172, v2, 11, v166
	global_load_lds_dwordx4 v168, s[28:29]
	s_add_i32 m0, s39, 0x12000
	s_add_u32 s2, s28, 0x40000
	v_mov_b32_e32 v165, 0
	global_load_lds_dwordx4 v172, s[28:29]
	s_addc_u32 s3, s29, 0
	s_add_i32 m0, s39, 0x14000
	v_lshl_add_u64 v[2:3], s[6:7], 0, v[164:165]
	global_load_lds_dwordx4 v168, s[2:3]
	s_add_i32 m0, s39, 0x16000
	v_mov_b32_e32 v167, v165
	global_load_lds_dwordx4 v172, s[2:3]
	v_lshl_add_u64 v[2:3], v[2:3], 0, v[166:167]
	s_mov_b32 m0, s39
	v_mov_b32_e32 v181, v165
	global_load_lds_dwordx4 v[2:3], off
	v_lshl_add_u64 v[2:3], s[6:7], 0, v[180:181]
	s_add_i32 s40, s39, 0x2000
	v_lshl_add_u64 v[2:3], v[2:3], 0, v[166:167]
	s_mov_b32 m0, s40
	v_mov_b32_e32 v185, v165
	global_load_lds_dwordx4 v[2:3], off
	s_add_i32 s41, s39, 0x4000
	v_lshl_add_u64 v[2:3], s[6:7], 0, v[184:185]
	v_lshl_add_u64 v[2:3], v[2:3], 0, v[166:167]
	s_mov_b32 m0, s41
	v_mov_b32_e32 v183, v165
	global_load_lds_dwordx4 v[2:3], off
	v_lshl_add_u64 v[2:3], s[6:7], 0, v[182:183]
	s_add_i32 s42, s39, 0x6000
	v_lshl_add_u64 v[2:3], v[2:3], 0, v[166:167]
	s_mov_b32 m0, s42
	v_mov_b32_e32 v169, v165
	global_load_lds_dwordx4 v[2:3], off
	v_mov_b32_e32 v173, v165
	s_cmp_eq_u32 s0, 1
	s_mov_b32 s62, 0
	s_mov_b32 s43, 0x10000
	v_lshl_add_u64 v[2:3], s[28:29], 0, v[168:169]
	s_cselect_b64 s[8:9], -1, 0
	s_cmp_lg_u32 s0, 1
	v_lshl_add_u64 v[4:5], s[28:29], 0, v[172:173]
	s_cbranch_scc1 .LBB0_1410
	s_barrier
